# stack10 + resid_rows (XCD-local loops): the two wave_sum butterflies per row (12 ds_bpermute round trips) replaced by DPP row reductions + v_readlane of the four row totals
# baseline (speedup 1.0000x reference)
; __device__ __forceinline__ float wave_sum(float v) {
; #pragma unroll
;     for (int o = 1; o < 64; o <<= 1) v += __shfl_xor(v, o);
;     return v;
; __device__ __forceinline__ void resid_rows(bf16* X, const bf16* Y, const float* PART, const float* gpost, float* RSv, float* RQv, float* fout, unsigned char* XQv, int m0, int mstep, int lane, int M_end = M) {
;     ...
;         const float ps = wave_sum(cp); const float rs1 = 1.f / sqrtf(ps * (1.f / DM) + NORM_EPS);
;         f32x4 v[8]; float s = 0.f;
; #pragma unroll
;         for (int j = 0; j < 8; ++j) { const v2u x = cx[j], y = cy[j];
;             v[j].x = bflo(x.x) + bflo(y.x) * rs1 * g[j].x; v[j].y = bfhi(x.x) + bfhi(y.x) * rs1 * g[j].y; v[j].z = bflo(x.y) + bflo(y.y) * rs1 * g[j].z; v[j].w = bfhi(x.y) + bfhi(y.y) * rs1 * g[j].w;
;             s += (v[j].x * v[j].x + v[j].y * v[j].y) + (v[j].z * v[j].z + v[j].w * v[j].w); }
.LBB0_1027:
	s_nop 1
	v_add_f32_dpp v1, v108, v108 quad_perm:[1,0,3,2] row_mask:0xf bank_mask:0xf
	s_nop 1
	v_add_f32_dpp v1, v1, v1 quad_perm:[2,3,0,1] row_mask:0xf bank_mask:0xf
	s_nop 1
	v_add_f32_dpp v1, v1, v1 row_half_mirror row_mask:0xf bank_mask:0xf
	s_nop 1
	v_add_f32_dpp v1, v1, v1 row_mirror row_mask:0xf bank_mask:0xf
	s_nop 1
	v_readlane_b32 s100, v1, 0
	v_readlane_b32 s101, v1, 16
	s_nop 1
	v_mov_b32_e32 v210, s100
	v_add_f32_e32 v210, s101, v210
	v_readlane_b32 s100, v1, 32
	v_readlane_b32 s101, v1, 48
	s_nop 1
	v_add_f32_e32 v210, s100, v210
	v_add_f32_e32 v1, s101, v210
	v_lshlrev_b32_e32 v122, 16, v100
	v_and_b32_e32 v123, 0xffff0000, v100
	v_lshlrev_b32_e32 v124, 16, v101
	v_lshlrev_b32_e32 v118, 16, v104
	v_and_b32_e32 v119, 0xffff0000, v104
	v_lshlrev_b32_e32 v104, 16, v105
	v_and_b32_e32 v105, 0xffff0000, v105
	v_lshlrev_b32_e32 v108, 16, v106
	v_and_b32_e32 v109, 0xffff0000, v106
	v_lshlrev_b32_e32 v106, 16, v107
	v_and_b32_e32 v107, 0xffff0000, v107
	v_lshlrev_b32_e32 v120, 16, v102
	v_and_b32_e32 v121, 0xffff0000, v102
	v_lshlrev_b32_e32 v102, 16, v103
	v_and_b32_e32 v103, 0xffff0000, v103
	s_mov_b32 s3, 0x23800000
	v_fmamk_f32 v1, v1, 0x3a000000, v240
	v_mul_f32_e32 v2, 0x4f800000, v1
	v_cmp_gt_f32_e32 vcc, s82, v1
	s_nop 1
	v_cndmask_b32_e32 v1, v1, v2, vcc
	v_sqrt_f32_e32 v2, v1
	s_nop 0
	v_add_u32_e32 v100, -1, v2
	v_add_u32_e32 v117, 1, v2
	v_fma_f32 v125, -v100, v2, v1
	v_fma_f32 v126, -v117, v2, v1
	v_cmp_ge_f32_e64 s[42:43], 0, v125
	v_and_b32_e32 v125, 0xffff0000, v101
	s_nop 0
	v_cndmask_b32_e64 v2, v2, v100, s[42:43]
	v_cmp_lt_f32_e64 s[42:43], 0, v126
	s_nop 1
	v_cndmask_b32_e64 v2, v2, v117, s[42:43]
	v_mul_f32_e32 v100, 0x37800000, v2
	v_cndmask_b32_e32 v2, v2, v100, vcc
	v_cmp_class_f32_e32 vcc, v1, v241
	s_nop 1
	v_cndmask_b32_e32 v1, v2, v1, vcc
	v_div_scale_f32 v2, s[4:5], v1, v1, 1.0
	v_rcp_f32_e32 v100, v2
	v_div_scale_f32 v101, vcc, 1.0, v1, 1.0
	v_fma_f32 v117, -v2, v100, 1.0
	v_fmac_f32_e32 v100, v117, v100
	v_mul_f32_e32 v117, v101, v100
	v_fma_f32 v126, -v2, v117, v101
	v_fmac_f32_e32 v117, v126, v100
	v_fma_f32 v2, -v2, v117, v101
	v_div_fmas_f32 v2, v2, v100, v117
	v_div_fixup_f32 v2, v2, v1, 1.0
	v_pk_mul_f32 v[100:101], v[2:3], v[118:119] op_sel_hi:[0,1]
	v_pk_mul_f32 v[104:105], v[2:3], v[104:105] op_sel_hi:[0,1]
	v_pk_mul_f32 v[118:119], v[2:3], v[122:123] op_sel_hi:[0,1]
	v_pk_fma_f32 v[108:109], v[4:5], v[100:101], v[108:109]
	v_pk_fma_f32 v[106:107], v[6:7], v[104:105], v[106:107]
	v_pk_fma_f32 v[100:101], v[8:9], v[118:119], v[120:121]
	v_pk_mul_f32 v[104:105], v[2:3], v[124:125] op_sel_hi:[0,1]
	v_lshlrev_b32_e32 v118, 16, v96
	v_and_b32_e32 v119, 0xffff0000, v96
	v_pk_fma_f32 v[104:105], v[10:11], v[104:105], v[102:103]
	v_lshlrev_b32_e32 v102, 16, v98
	v_and_b32_e32 v103, 0xffff0000, v98
	v_pk_mul_f32 v[118:119], v[2:3], v[118:119] op_sel_hi:[0,1]
	v_lshlrev_b32_e32 v96, 16, v97
	v_and_b32_e32 v97, 0xffff0000, v97
	v_pk_fma_f32 v[102:103], v[12:13], v[118:119], v[102:103]
	v_lshlrev_b32_e32 v98, 16, v99
	v_and_b32_e32 v99, 0xffff0000, v99
	v_pk_mul_f32 v[96:97], v[2:3], v[96:97] op_sel_hi:[0,1]
	v_lshlrev_b32_e32 v118, 16, v92
	v_and_b32_e32 v119, 0xffff0000, v92
	v_pk_fma_f32 v[98:99], v[14:15], v[96:97], v[98:99]
	v_lshlrev_b32_e32 v96, 16, v94
	v_and_b32_e32 v97, 0xffff0000, v94
	v_pk_mul_f32 v[118:119], v[2:3], v[118:119] op_sel_hi:[0,1]
	v_lshlrev_b32_e32 v92, 16, v93
	v_and_b32_e32 v93, 0xffff0000, v93
	v_pk_fma_f32 v[96:97], v[16:17], v[118:119], v[96:97]
	v_lshlrev_b32_e32 v94, 16, v95
	v_and_b32_e32 v95, 0xffff0000, v95
	v_pk_mul_f32 v[92:93], v[2:3], v[92:93] op_sel_hi:[0,1]
	v_lshlrev_b32_e32 v118, 16, v88
	v_and_b32_e32 v119, 0xffff0000, v88
	v_pk_fma_f32 v[94:95], v[18:19], v[92:93], v[94:95]
	v_lshlrev_b32_e32 v92, 16, v90
	v_and_b32_e32 v93, 0xffff0000, v90
	v_pk_mul_f32 v[118:119], v[2:3], v[118:119] op_sel_hi:[0,1]
	v_lshlrev_b32_e32 v88, 16, v89
	v_and_b32_e32 v89, 0xffff0000, v89
	v_pk_fma_f32 v[92:93], v[20:21], v[118:119], v[92:93]
	v_lshlrev_b32_e32 v90, 16, v91
	v_and_b32_e32 v91, 0xffff0000, v91
	v_pk_mul_f32 v[88:89], v[2:3], v[88:89] op_sel_hi:[0,1]
	v_lshlrev_b32_e32 v118, 16, v84
	v_and_b32_e32 v119, 0xffff0000, v84
	v_pk_fma_f32 v[90:91], v[22:23], v[88:89], v[90:91]
	v_lshlrev_b32_e32 v88, 16, v86
	v_and_b32_e32 v89, 0xffff0000, v86
	v_pk_mul_f32 v[118:119], v[2:3], v[118:119] op_sel_hi:[0,1]
	v_lshlrev_b32_e32 v84, 16, v85
	v_and_b32_e32 v85, 0xffff0000, v85
	v_pk_fma_f32 v[88:89], v[24:25], v[118:119], v[88:89]
	v_lshlrev_b32_e32 v86, 16, v87
	v_and_b32_e32 v87, 0xffff0000, v87
	v_pk_mul_f32 v[84:85], v[2:3], v[84:85] op_sel_hi:[0,1]
	v_lshlrev_b32_e32 v118, 16, v80
	v_and_b32_e32 v119, 0xffff0000, v80
	v_pk_fma_f32 v[86:87], v[26:27], v[84:85], v[86:87]
	v_lshlrev_b32_e32 v84, 16, v82
	v_and_b32_e32 v85, 0xffff0000, v82
	v_pk_mul_f32 v[118:119], v[2:3], v[118:119] op_sel_hi:[0,1]
	v_lshlrev_b32_e32 v80, 16, v81
	v_and_b32_e32 v81, 0xffff0000, v81
	v_pk_fma_f32 v[84:85], v[28:29], v[118:119], v[84:85]
	v_lshlrev_b32_e32 v82, 16, v83
	v_and_b32_e32 v83, 0xffff0000, v83
	v_pk_mul_f32 v[80:81], v[2:3], v[80:81] op_sel_hi:[0,1]
	v_lshlrev_b32_e32 v118, 16, v76
	v_and_b32_e32 v119, 0xffff0000, v76
	v_lshlrev_b32_e32 v76, 16, v77
	v_and_b32_e32 v77, 0xffff0000, v77
	v_pk_fma_f32 v[82:83], v[30:31], v[80:81], v[82:83]
	v_lshlrev_b32_e32 v80, 16, v78
	v_and_b32_e32 v81, 0xffff0000, v78
	v_pk_mul_f32 v[118:119], v[2:3], v[118:119] op_sel_hi:[0,1]
	v_lshlrev_b32_e32 v78, 16, v79
	v_and_b32_e32 v79, 0xffff0000, v79
	v_pk_mul_f32 v[76:77], v[2:3], v[76:77] op_sel_hi:[0,1]
	v_pk_mul_f32 v[120:121], v[100:101], v[100:101]
	v_pk_mul_f32 v[122:123], v[104:105], v[104:105]
; #define GAS __attribute__((address_space(1)))
; __device__ __forceinline__ unsigned pk2(float lo, float hi) { f32x2_t_ v = {lo, hi}; bf16x2_t_ b = __builtin_convertvector(v, bf16x2_t_); return __builtin_bit_cast(unsigned, b); }
; __device__ __forceinline__ float quant_row(const f32x4 (&v)[8], unsigned char* xq, int lane) {
;     float mx = 0.f;
; #pragma unroll
;     for (int j = 0; j < 8; ++j) mx = __builtin_fmaxf(mx, __builtin_fmaxf(__builtin_fmaxf(__builtin_fabsf(v[j].x), __builtin_fabsf(v[j].y)), __builtin_fmaxf(__builtin_fabsf(v[j].z), __builtin_fabsf(v[j].w))));
;     mx = __builtin_fmaxf(wave_max(mx), 1e-20f);
; __device__ __forceinline__ void resid_rows(bf16* X, const bf16* Y, const float* PART, const float* gpost, float* RSv, float* RQv, float* fout, unsigned char* XQv, int m0, int mstep, int lane, int M_end = M) {
;     ...
;             s += (v[j].x * v[j].x + v[j].y * v[j].y) + (v[j].z * v[j].z + v[j].w * v[j].w); }
;         if (fout) { GAS f32x4* xo = (GAS f32x4*)(fout + (size_t)m * DM) + lane;
; #pragma unroll
;             for (int j = 0; j < 8; ++j) xo[64 * j] = v[j]; }
;         else { s = wave_sum(s); GAS v2u* xw = (GAS v2u*)(X + (size_t)m * DM) + lane;
; #pragma unroll
;             for (int j = 0; j < 8; ++j) { v2u w; w.x = pk2(v[j].x, v[j].y); w.y = pk2(v[j].z, v[j].w); xw[64 * j] = w; }
;             const float dq = quant_row(v, XQv + (size_t)m * DM, lane);
	v_pk_fma_f32 v[80:81], v[32:33], v[118:119], v[80:81]
	v_pk_fma_f32 v[76:77], v[34:35], v[76:77], v[78:79]
	v_pk_mul_f32 v[78:79], v[108:109], v[108:109]
	v_pk_mul_f32 v[118:119], v[106:107], v[106:107]
	v_add_f32_e32 v1, v123, v122
	v_add_f32_e32 v2, v120, v121
	v_add_f32_e32 v1, v2, v1
	v_add_f32_e32 v2, v119, v118
	v_add_f32_e32 v78, v78, v79
	v_pk_mul_f32 v[124:125], v[102:103], v[102:103]
	v_pk_mul_f32 v[126:127], v[98:99], v[98:99]
	v_add_f32_e32 v2, v78, v2
	v_add_f32_e32 v1, v2, v1
	v_add_f32_e32 v2, v127, v126
	v_add_f32_e32 v78, v124, v125
	v_pk_mul_f32 v[128:129], v[96:97], v[96:97]
	v_pk_mul_f32 v[130:131], v[94:95], v[94:95]
	v_add_f32_e32 v2, v78, v2
	v_add_f32_e32 v1, v2, v1
	v_add_f32_e32 v2, v131, v130
	v_add_f32_e32 v78, v128, v129
	v_pk_mul_f32 v[132:133], v[92:93], v[92:93]
	v_pk_mul_f32 v[134:135], v[90:91], v[90:91]
	v_add_f32_e32 v2, v78, v2
	v_add_f32_e32 v1, v2, v1
	v_add_f32_e32 v2, v135, v134
	v_add_f32_e32 v78, v132, v133
	v_pk_mul_f32 v[136:137], v[88:89], v[88:89]
	v_pk_mul_f32 v[138:139], v[86:87], v[86:87]
	v_add_f32_e32 v2, v78, v2
	v_add_f32_e32 v1, v2, v1
	v_add_f32_e32 v2, v139, v138
	v_add_f32_e32 v78, v136, v137
	v_pk_mul_f32 v[140:141], v[84:85], v[84:85]
	v_pk_mul_f32 v[142:143], v[82:83], v[82:83]
	v_add_f32_e32 v2, v78, v2
	v_add_f32_e32 v1, v2, v1
	v_add_f32_e32 v2, v143, v142
	v_add_f32_e32 v78, v140, v141
	v_pk_mul_f32 v[144:145], v[80:81], v[80:81]
	v_pk_mul_f32 v[146:147], v[76:77], v[76:77]
	v_add_f32_e32 v2, v78, v2
	v_add_f32_e32 v1, v2, v1
	v_add_f32_e32 v2, v147, v146
	v_add_f32_e32 v78, v144, v145
	v_add_f32_e32 v2, v78, v2
	v_add_f32_e32 v1, v2, v1
	s_nop 1
	v_add_f32_dpp v1, v1, v1 quad_perm:[1,0,3,2] row_mask:0xf bank_mask:0xf
	s_nop 1
	v_add_f32_dpp v1, v1, v1 quad_perm:[2,3,0,1] row_mask:0xf bank_mask:0xf
	s_nop 1
	v_add_f32_dpp v1, v1, v1 row_half_mirror row_mask:0xf bank_mask:0xf
	s_nop 1
	v_add_f32_dpp v1, v1, v1 row_mirror row_mask:0xf bank_mask:0xf
	s_nop 1
	v_readlane_b32 s100, v1, 0
	v_readlane_b32 s101, v1, 16
	s_nop 1
	v_mov_b32_e32 v210, s100
	v_add_f32_e32 v210, s101, v210
	v_readlane_b32 s100, v1, 32
	v_readlane_b32 s101, v1, 48
	s_nop 1
	v_add_f32_e32 v210, s100, v210
	v_add_f32_e32 v1, s101, v210
	v_max_f32_e64 v78, |v104|, |v105|
	v_max3_f32 v78, |v100|, |v101|, v78
	v_max_f32_e64 v79, |v94|, |v95|
	v_max3_f32 v79, |v96|, |v97|, v79
	v_cvt_pk_bf16_f32 v118, v108, v109
	v_cvt_pk_bf16_f32 v119, v106, v107
	v_max_f32_e64 v2, |v106|, |v107|
	v_max3_f32 v2, |v108|, |v109|, v2
	v_max3_f32 v2, v2, 0, v78
	v_max_f32_e64 v78, |v98|, |v99|
	v_max3_f32 v78, |v102|, |v103|, v78
	v_max3_f32 v2, v2, v78, v79
	v_max_f32_e64 v78, |v90|, |v91|
	v_max_f32_e64 v79, |v86|, |v87|
	v_max3_f32 v78, |v92|, |v93|, v78
	v_max3_f32 v79, |v88|, |v89|, v79
	v_max3_f32 v2, v2, v78, v79
	v_max_f32_e64 v78, |v82|, |v83|
	v_max_f32_e64 v79, |v76|, |v77|
	v_max3_f32 v78, |v84|, |v85|, v78
	v_max3_f32 v79, |v80|, |v81|, v79
	v_max3_f32 v117, v2, v78, v79
	ds_bpermute_b32 v120, v111, v117
	v_lshl_add_u64 v[78:79], s[84:85], 0, v[38:39]
	s_waitcnt lgkmcnt(0)
	v_max_f32_e32 v120, v120, v120
	v_max_f32_e32 v117, v117, v120
	ds_bpermute_b32 v122, v112, v117
	v_add_co_u32_e32 v120, vcc, s3, v78
	v_cvt_pk_bf16_f32 v78, v100, v101
	s_nop 0
	v_addc_co_u32_e32 v121, vcc, 0, v79, vcc
	s_waitcnt vmcnt(0)
	global_store_dwordx2 v[120:121], v[118:119], off
	s_waitcnt lgkmcnt(0)
	v_max_f32_e32 v118, v122, v122
	v_max_f32_e32 v117, v117, v118
	ds_bpermute_b32 v118, v113, v117
	v_cvt_pk_bf16_f32 v79, v104, v105
	global_store_dwordx2 v[120:121], v[78:79], off offset:512
	v_cvt_pk_bf16_f32 v78, v102, v103
	v_cvt_pk_bf16_f32 v79, v98, v99
	global_store_dwordx2 v[120:121], v[78:79], off offset:1024
	s_waitcnt lgkmcnt(0)
	v_max_f32_e32 v78, v118, v118
	v_max_f32_e32 v117, v117, v78
	ds_bpermute_b32 v118, v114, v117
	v_cvt_pk_bf16_f32 v78, v96, v97
	v_cvt_pk_bf16_f32 v79, v94, v95
	global_store_dwordx2 v[120:121], v[78:79], off offset:1536
	v_cvt_pk_bf16_f32 v78, v92, v93
	s_waitcnt lgkmcnt(0)
	v_max_f32_e32 v79, v118, v118
	v_max_f32_e32 v117, v117, v79
	ds_bpermute_b32 v118, v115, v117
	v_cvt_pk_bf16_f32 v79, v90, v91
	global_store_dwordx2 v[120:121], v[78:79], off offset:2048
	v_cvt_pk_bf16_f32 v78, v88, v89
	v_cvt_pk_bf16_f32 v79, v86, v87
	s_waitcnt lgkmcnt(0)
	v_max_f32_e32 v118, v118, v118
	v_max_f32_e32 v117, v117, v118
	ds_bpermute_b32 v118, v116, v117
	global_store_dwordx2 v[120:121], v[78:79], off offset:2560
	v_cvt_pk_bf16_f32 v78, v84, v85
	v_cvt_pk_bf16_f32 v79, v82, v83
	s_mov_b32 s3, 0x1e3ce508
	global_store_dwordx2 v[120:121], v[78:79], off offset:3072
	s_waitcnt lgkmcnt(0)
; #define GAS __attribute__((address_space(1)))
; __device__ __forceinline__ float quant_row(const f32x4 (&v)[8], unsigned char* xq, int lane) {
;     float mx = 0.f;
; #pragma unroll
;     for (int j = 0; j < 8; ++j) mx = __builtin_fmaxf(mx, __builtin_fmaxf(__builtin_fmaxf(__builtin_fabsf(v[j].x), __builtin_fabsf(v[j].y)), __builtin_fmaxf(__builtin_fabsf(v[j].z), __builtin_fabsf(v[j].w))));
;     mx = __builtin_fmaxf(wave_max(mx), 1e-20f);
;     const float q = 127.0f / mx;
;     GAS unsigned* o4 = (GAS unsigned*)xq + lane;
; #pragma unroll
;     for (int j = 0; j < 8; ++j) o4[64 * j] = q4(v[j], q);
;     return mx * (1.0f / 127.0f);
; __device__ __forceinline__ void resid_rows(bf16* X, const bf16* Y, const float* PART, const float* gpost, float* RSv, float* RQv, float* fout, unsigned char* XQv, int m0, int mstep, int lane, int M_end = M) {
;     ...
;             const float dq = quant_row(v, XQv + (size_t)m * DM, lane);
;             if (lane == 0) { const float r = 1.f / sqrtf(s * (1.f / DM) + NORM_EPS); RSv[m] = r; RQv[m] = r * dq; } }
	v_max3_f32 v78, v117, v118, s3
	s_mov_b32 s3, 0x42fe0000
	v_div_scale_f32 v79, s[4:5], v78, v78, s3
	v_rcp_f32_e32 v117, v79
	v_cvt_pk_bf16_f32 v118, v80, v81
	v_cvt_pk_bf16_f32 v119, v76, v77
	global_store_dwordx2 v[120:121], v[118:119], off offset:3584
	v_fma_f32 v118, -v79, v117, 1.0
	v_fmac_f32_e32 v117, v118, v117
	v_div_scale_f32 v118, vcc, s3, v78, s3
	v_mul_f32_e32 v119, v118, v117
	v_fma_f32 v120, -v79, v119, v118
	v_fmac_f32_e32 v119, v120, v117
	v_fma_f32 v79, -v79, v119, v118
	v_div_fmas_f32 v79, v79, v117, v119
	v_div_fixup_f32 v79, v79, v78, s3
	v_mul_f32_e32 v109, v109, v79
	v_mul_f32_e32 v108, v108, v79
	v_rndne_f32_e32 v109, v109
	v_mul_f32_e32 v106, v106, v79
	v_mul_f32_e32 v107, v107, v79
	v_mul_f32_e32 v101, v101, v79
	v_rndne_f32_e32 v108, v108
	v_cvt_i32_f32_e32 v109, v109
	v_rndne_f32_e32 v106, v106
	v_rndne_f32_e32 v107, v107
	v_mul_f32_e32 v100, v100, v79
	v_rndne_f32_e32 v101, v101
	v_mul_f32_e32 v104, v104, v79
	v_mul_f32_e32 v105, v105, v79
	v_cvt_i32_f32_e32 v108, v108
	v_cvt_i32_f32_sdwa v106, v106 dst_sel:WORD_1 dst_unused:UNUSED_PAD src0_sel:DWORD
	v_cvt_i32_f32_e32 v107, v107
	v_rndne_f32_e32 v100, v100
	v_cvt_i32_f32_e32 v101, v101
	v_rndne_f32_e32 v104, v104
	v_rndne_f32_e32 v105, v105
	v_cvt_i32_f32_e32 v100, v100
	v_cvt_i32_f32_sdwa v104, v104 dst_sel:WORD_1 dst_unused:UNUSED_PAD src0_sel:DWORD
	v_cvt_i32_f32_e32 v105, v105
	v_lshlrev_b32_e32 v109, 8, v109
	v_lshl_add_u64 v[118:119], s[84:85], 0, v[36:37]
	v_and_b32_e32 v109, 0xff00, v109
	v_and_b32_e32 v106, 0xff0000, v106
	v_perm_b32 v107, v107, v108, s17
	s_mov_b32 s3, 0x8800000
	v_lshlrev_b32_e32 v101, 8, v101
	v_or3_b32 v108, v107, v109, v106
	v_add_co_u32_e32 v106, vcc, s3, v118
	v_and_b32_e32 v101, 0xff00, v101
	v_and_b32_e32 v104, 0xff0000, v104
	v_perm_b32 v100, v105, v100, s17
	v_addc_co_u32_e32 v107, vcc, 0, v119, vcc
	v_or3_b32 v100, v100, v101, v104
	v_mul_f32_e32 v101, v103, v79
	v_mul_f32_e32 v97, v97, v79
	v_mul_f32_e32 v93, v93, v79
	v_mul_f32_e32 v89, v89, v79
	v_mul_f32_e32 v85, v85, v79
	v_mul_f32_e32 v81, v81, v79
	global_store_dword v[106:107], v100, off offset:256
	v_mul_f32_e32 v100, v102, v79
	v_rndne_f32_e32 v101, v101
	v_mul_f32_e32 v98, v98, v79
	v_mul_f32_e32 v99, v99, v79
	v_mul_f32_e32 v96, v96, v79
	v_rndne_f32_e32 v97, v97
	v_mul_f32_e32 v94, v94, v79
	v_mul_f32_e32 v95, v95, v79
	v_mul_f32_e32 v92, v92, v79
	v_rndne_f32_e32 v93, v93
	v_mul_f32_e32 v90, v90, v79
	v_mul_f32_e32 v91, v91, v79
	v_mul_f32_e32 v88, v88, v79
	v_rndne_f32_e32 v89, v89
	v_mul_f32_e32 v86, v86, v79
	v_mul_f32_e32 v87, v87, v79
	v_mul_f32_e32 v84, v84, v79
	v_rndne_f32_e32 v85, v85
	v_mul_f32_e32 v82, v82, v79
	v_mul_f32_e32 v83, v83, v79
	v_mul_f32_e32 v80, v80, v79
	v_rndne_f32_e32 v81, v81
	v_mul_f32_e32 v76, v76, v79
	v_mul_f32_e32 v77, v77, v79
	v_rndne_f32_e32 v100, v100
	v_cvt_i32_f32_e32 v101, v101
	v_rndne_f32_e32 v98, v98
	v_rndne_f32_e32 v99, v99
	v_rndne_f32_e32 v96, v96
	v_cvt_i32_f32_e32 v97, v97
	v_rndne_f32_e32 v94, v94
	v_rndne_f32_e32 v95, v95
	v_rndne_f32_e32 v92, v92
	v_cvt_i32_f32_e32 v93, v93
	v_rndne_f32_e32 v90, v90
	v_rndne_f32_e32 v91, v91
	v_rndne_f32_e32 v88, v88
	v_cvt_i32_f32_e32 v89, v89
	v_rndne_f32_e32 v86, v86
	v_rndne_f32_e32 v87, v87
	v_rndne_f32_e32 v84, v84
	v_cvt_i32_f32_e32 v85, v85
	v_rndne_f32_e32 v82, v82
	v_rndne_f32_e32 v83, v83
	v_rndne_f32_e32 v80, v80
	v_cvt_i32_f32_e32 v81, v81
	v_rndne_f32_e32 v76, v76
	v_rndne_f32_e32 v77, v77
	v_cvt_i32_f32_e32 v100, v100
	v_cvt_i32_f32_sdwa v98, v98 dst_sel:WORD_1 dst_unused:UNUSED_PAD src0_sel:DWORD
	v_cvt_i32_f32_e32 v99, v99
	v_cvt_i32_f32_e32 v96, v96
	v_cvt_i32_f32_sdwa v94, v94 dst_sel:WORD_1 dst_unused:UNUSED_PAD src0_sel:DWORD
	v_cvt_i32_f32_e32 v95, v95
	v_cvt_i32_f32_e32 v92, v92
	v_cvt_i32_f32_sdwa v90, v90 dst_sel:WORD_1 dst_unused:UNUSED_PAD src0_sel:DWORD
	v_cvt_i32_f32_e32 v91, v91
	v_cvt_i32_f32_e32 v88, v88
	v_cvt_i32_f32_sdwa v86, v86 dst_sel:WORD_1 dst_unused:UNUSED_PAD src0_sel:DWORD
	v_cvt_i32_f32_e32 v87, v87
	v_cvt_i32_f32_e32 v84, v84
	v_cvt_i32_f32_sdwa v82, v82 dst_sel:WORD_1 dst_unused:UNUSED_PAD src0_sel:DWORD
	v_cvt_i32_f32_e32 v83, v83
	v_cvt_i32_f32_e32 v80, v80
	v_cvt_i32_f32_sdwa v76, v76 dst_sel:WORD_1 dst_unused:UNUSED_PAD src0_sel:DWORD
	v_cvt_i32_f32_e32 v77, v77
	v_lshlrev_b32_e32 v101, 8, v101
	v_lshlrev_b32_e32 v97, 8, v97
	v_lshlrev_b32_e32 v93, 8, v93
	v_lshlrev_b32_e32 v89, 8, v89
	v_lshlrev_b32_e32 v85, 8, v85
	v_lshlrev_b32_e32 v79, 8, v81
	v_and_b32_e32 v101, 0xff00, v101
	v_and_b32_e32 v98, 0xff0000, v98
	v_perm_b32 v99, v99, v100, s17
	v_and_b32_e32 v97, 0xff00, v97
	v_and_b32_e32 v94, 0xff0000, v94
	v_perm_b32 v95, v95, v96, s17
	v_and_b32_e32 v93, 0xff00, v93
	v_and_b32_e32 v90, 0xff0000, v90
	v_perm_b32 v91, v91, v92, s17
	v_and_b32_e32 v89, 0xff00, v89
	v_and_b32_e32 v86, 0xff0000, v86
	v_perm_b32 v87, v87, v88, s17
	v_and_b32_e32 v85, 0xff00, v85
	v_and_b32_e32 v82, 0xff0000, v82
	v_perm_b32 v83, v83, v84, s17
	v_and_b32_e32 v79, 0xff00, v79
	v_and_b32_e32 v76, 0xff0000, v76
	v_perm_b32 v77, v77, v80, s17
	v_or3_b32 v98, v99, v101, v98
	v_or3_b32 v94, v95, v97, v94
	v_or3_b32 v90, v91, v93, v90
	v_or3_b32 v86, v87, v89, v86
	v_or3_b32 v82, v83, v85, v82
	v_or3_b32 v76, v77, v79, v76
	global_store_dword v[106:107], v108, off
	global_store_dword v[106:107], v98, off offset:512
	global_store_dword v[106:107], v94, off offset:768
	global_store_dword v[106:107], v90, off offset:1024
	global_store_dword v[106:107], v86, off offset:1280
	global_store_dword v[106:107], v82, off offset:1536
	global_store_dword v[106:107], v76, off offset:1792
	s_and_saveexec_b64 s[48:49], s[40:41]
	s_cbranch_execz .LBB0_1022
	v_fmamk_f32 v1, v1, 0x3a000000, v240
	v_mul_f32_e32 v2, 0x4f800000, v1
	v_cmp_gt_f32_e32 vcc, s82, v1
	s_nop 1
	v_cndmask_b32_e32 v1, v1, v2, vcc
	v_sqrt_f32_e32 v2, v1
	s_nop 0
	v_add_u32_e32 v76, -1, v2
	v_fma_f32 v79, -v76, v2, v1
	v_add_u32_e32 v77, 1, v2
	v_cmp_ge_f32_e64 s[42:43], 0, v79
	s_nop 1
	v_cndmask_b32_e64 v76, v2, v76, s[42:43]
	v_fma_f32 v2, -v77, v2, v1
	v_cmp_lt_f32_e64 s[42:43], 0, v2
	s_nop 1
	v_cndmask_b32_e64 v2, v76, v77, s[42:43]
	v_mul_f32_e32 v76, 0x37800000, v2
	v_cndmask_b32_e32 v2, v2, v76, vcc
	v_cmp_class_f32_e32 vcc, v1, v241
	v_mul_f32_e32 v77, 0x3c010204, v78
	s_nop 0
	v_cndmask_b32_e32 v1, v2, v1, vcc
	v_div_scale_f32 v2, s[4:5], v1, v1, 1.0
	v_rcp_f32_e32 v76, v2
	s_add_u32 s4, s84, s44
	s_addc_u32 s5, s85, s45
	v_fma_f32 v78, -v2, v76, 1.0
	v_fmac_f32_e32 v76, v78, v76
	v_div_scale_f32 v78, vcc, 1.0, v1, 1.0
	v_mul_f32_e32 v79, v78, v76
	v_fma_f32 v80, -v2, v79, v78
	v_fmac_f32_e32 v79, v80, v76
	v_fma_f32 v2, -v2, v79, v78
	v_div_fmas_f32 v2, v2, v76, v79
	v_div_fixup_f32 v1, v2, v1, 1.0
	global_store_dword v236, v1, s[4:5]
	v_mul_f32_e32 v1, v77, v1
	global_store_dword v237, v1, s[4:5]
	s_branch .LBB0_1022

; #define GAS __attribute__((address_space(1)))
; __device__ __forceinline__ void resid_rows(bf16* X, const bf16* Y, const float* PART, const float* gpost, float* RSv, float* RQv, float* fout, unsigned char* XQv, int m0, int mstep, int lane, int M_end = M) {
;     ...
;         const float ps = wave_sum(cp); const float rs1 = 1.f / sqrtf(ps * (1.f / DM) + NORM_EPS);
;         f32x4 v[8]; float s = 0.f;
; #pragma unroll
;         for (int j = 0; j < 8; ++j) { const v2u x = cx[j], y = cy[j];
;             v[j].x = bflo(x.x) + bflo(y.x) * rs1 * g[j].x; v[j].y = bfhi(x.x) + bfhi(y.x) * rs1 * g[j].y; v[j].z = bflo(x.y) + bflo(y.y) * rs1 * g[j].z; v[j].w = bfhi(x.y) + bfhi(y.y) * rs1 * g[j].w;
;             s += (v[j].x * v[j].x + v[j].y * v[j].y) + (v[j].z * v[j].z + v[j].w * v[j].w); }
;         if (fout) { GAS f32x4* xo = (GAS f32x4*)(fout + (size_t)m * DM) + lane;
; #pragma unroll
;             for (int j = 0; j < 8; ++j) xo[64 * j] = v[j]; }
.LBB0_1368:
	s_nop 1
	v_add_f32_dpp v1, v119, v119 quad_perm:[1,0,3,2] row_mask:0xf bank_mask:0xf
	s_nop 1
	v_add_f32_dpp v1, v1, v1 quad_perm:[2,3,0,1] row_mask:0xf bank_mask:0xf
	s_nop 1
	v_add_f32_dpp v1, v1, v1 row_half_mirror row_mask:0xf bank_mask:0xf
	s_nop 1
	v_add_f32_dpp v1, v1, v1 row_mirror row_mask:0xf bank_mask:0xf
	s_nop 1
	v_readlane_b32 s100, v1, 0
	v_readlane_b32 s101, v1, 16
	s_nop 1
	v_mov_b32_e32 v210, s100
	v_add_f32_e32 v210, s101, v210
	v_readlane_b32 s100, v1, 32
	v_readlane_b32 s101, v1, 48
	s_nop 1
	v_add_f32_e32 v210, s100, v210
	v_add_f32_e32 v1, s101, v210
	v_and_b32_e32 v121, 0xffff0000, v38
	v_fmamk_f32 v1, v1, 0x3a000000, v240
	v_cmp_gt_f32_e32 vcc, s82, v1
	v_mul_f32_e32 v2, 0x4f800000, v1
	s_nop 0
	v_cndmask_b32_e32 v1, v1, v2, vcc
	v_sqrt_f32_e32 v2, v1
	s_nop 0
	v_add_u32_e32 v36, -1, v2
	v_fma_f32 v37, -v36, v2, v1
	v_cmp_ge_f32_e64 s[40:41], 0, v37
	v_add_u32_e32 v37, 1, v2
	s_nop 0
	v_cndmask_b32_e64 v36, v2, v36, s[40:41]
	v_fma_f32 v2, -v37, v2, v1
	v_cmp_lt_f32_e64 s[40:41], 0, v2
	s_nop 1
	v_cndmask_b32_e64 v2, v36, v37, s[40:41]
	v_mul_f32_e32 v36, 0x37800000, v2
	v_cndmask_b32_e32 v2, v2, v36, vcc
	v_cmp_class_f32_e32 vcc, v1, v241
	s_nop 1
	v_cndmask_b32_e32 v1, v2, v1, vcc
	v_div_scale_f32 v2, s[18:19], v1, v1, 1.0
	v_rcp_f32_e32 v36, v2
	s_nop 0
	v_fma_f32 v37, -v2, v36, 1.0
	v_fmac_f32_e32 v36, v37, v36
	v_div_scale_f32 v37, vcc, 1.0, v1, 1.0
	v_mul_f32_e32 v119, v37, v36
	v_fma_f32 v120, -v2, v119, v37
	v_fmac_f32_e32 v119, v120, v36
	v_fma_f32 v2, -v2, v119, v37
	v_div_fmas_f32 v2, v2, v36, v119
	v_div_fixup_f32 v2, v2, v1, 1.0
	v_lshlrev_b32_e32 v120, 16, v38
	v_lshlrev_b32_e32 v36, 16, v40
	v_and_b32_e32 v37, 0xffff0000, v40
	v_pk_mul_f32 v[120:121], v[2:3], v[120:121] op_sel_hi:[0,1]
	v_lshlrev_b32_e32 v38, 16, v39
	v_and_b32_e32 v39, 0xffff0000, v39
	v_pk_fma_f32 v[36:37], v[4:5], v[120:121], v[36:37]
	v_lshlrev_b32_e32 v40, 16, v41
	v_and_b32_e32 v41, 0xffff0000, v41
	v_pk_mul_f32 v[38:39], v[2:3], v[38:39] op_sel_hi:[0,1]
	v_lshlrev_b32_e32 v120, 16, v42
	v_and_b32_e32 v121, 0xffff0000, v42
	v_pk_fma_f32 v[38:39], v[6:7], v[38:39], v[40:41]
	v_lshlrev_b32_e32 v40, 16, v44
	v_and_b32_e32 v41, 0xffff0000, v44
	v_pk_mul_f32 v[120:121], v[2:3], v[120:121] op_sel_hi:[0,1]
	v_lshlrev_b32_e32 v42, 16, v43
	v_and_b32_e32 v43, 0xffff0000, v43
	v_pk_fma_f32 v[40:41], v[8:9], v[120:121], v[40:41]
	v_lshlrev_b32_e32 v44, 16, v45
	v_and_b32_e32 v45, 0xffff0000, v45
	v_pk_mul_f32 v[42:43], v[2:3], v[42:43] op_sel_hi:[0,1]
	v_lshlrev_b32_e32 v120, 16, v46
	v_and_b32_e32 v121, 0xffff0000, v46
	v_pk_fma_f32 v[42:43], v[10:11], v[42:43], v[44:45]
	v_lshlrev_b32_e32 v44, 16, v48
	v_and_b32_e32 v45, 0xffff0000, v48
	v_pk_mul_f32 v[120:121], v[2:3], v[120:121] op_sel_hi:[0,1]
	v_lshlrev_b32_e32 v46, 16, v47
	v_and_b32_e32 v47, 0xffff0000, v47
	v_pk_fma_f32 v[44:45], v[12:13], v[120:121], v[44:45]
	v_lshlrev_b32_e32 v48, 16, v49
	v_and_b32_e32 v49, 0xffff0000, v49
	v_pk_mul_f32 v[46:47], v[2:3], v[46:47] op_sel_hi:[0,1]
	v_lshlrev_b32_e32 v120, 16, v50
	v_and_b32_e32 v121, 0xffff0000, v50
	v_pk_fma_f32 v[46:47], v[14:15], v[46:47], v[48:49]
	v_lshlrev_b32_e32 v48, 16, v52
	v_and_b32_e32 v49, 0xffff0000, v52
	v_pk_mul_f32 v[120:121], v[2:3], v[120:121] op_sel_hi:[0,1]
	v_lshlrev_b32_e32 v50, 16, v51
	v_and_b32_e32 v51, 0xffff0000, v51
	v_pk_fma_f32 v[48:49], v[16:17], v[120:121], v[48:49]
	v_lshlrev_b32_e32 v52, 16, v53
	v_and_b32_e32 v53, 0xffff0000, v53
	v_pk_mul_f32 v[50:51], v[2:3], v[50:51] op_sel_hi:[0,1]
	v_lshlrev_b32_e32 v120, 16, v54
	v_and_b32_e32 v121, 0xffff0000, v54
	v_pk_fma_f32 v[50:51], v[18:19], v[50:51], v[52:53]
	v_lshlrev_b32_e32 v52, 16, v56
	v_and_b32_e32 v53, 0xffff0000, v56
	v_pk_mul_f32 v[120:121], v[2:3], v[120:121] op_sel_hi:[0,1]
	v_lshlrev_b32_e32 v54, 16, v55
	v_and_b32_e32 v55, 0xffff0000, v55
	v_pk_fma_f32 v[52:53], v[20:21], v[120:121], v[52:53]
	v_lshlrev_b32_e32 v56, 16, v57
	v_and_b32_e32 v57, 0xffff0000, v57
	v_pk_mul_f32 v[54:55], v[2:3], v[54:55] op_sel_hi:[0,1]
	v_lshlrev_b32_e32 v120, 16, v58
	v_and_b32_e32 v121, 0xffff0000, v58
	v_pk_fma_f32 v[54:55], v[22:23], v[54:55], v[56:57]
	v_lshlrev_b32_e32 v56, 16, v60
	v_and_b32_e32 v57, 0xffff0000, v60
	v_pk_mul_f32 v[120:121], v[2:3], v[120:121] op_sel_hi:[0,1]
	v_lshlrev_b32_e32 v58, 16, v59
	v_and_b32_e32 v59, 0xffff0000, v59
	v_pk_fma_f32 v[56:57], v[24:25], v[120:121], v[56:57]
	v_lshlrev_b32_e32 v60, 16, v61
	v_and_b32_e32 v61, 0xffff0000, v61
	v_pk_mul_f32 v[58:59], v[2:3], v[58:59] op_sel_hi:[0,1]
	v_lshlrev_b32_e32 v120, 16, v62
	v_and_b32_e32 v121, 0xffff0000, v62
	v_pk_fma_f32 v[58:59], v[26:27], v[58:59], v[60:61]
	v_lshlrev_b32_e32 v60, 16, v64
	v_and_b32_e32 v61, 0xffff0000, v64
	v_pk_mul_f32 v[120:121], v[2:3], v[120:121] op_sel_hi:[0,1]
	v_lshlrev_b32_e32 v62, 16, v63
	v_and_b32_e32 v63, 0xffff0000, v63
	v_pk_fma_f32 v[60:61], v[28:29], v[120:121], v[60:61]
	v_lshlrev_b32_e32 v64, 16, v65
	v_and_b32_e32 v65, 0xffff0000, v65
	v_pk_mul_f32 v[62:63], v[2:3], v[62:63] op_sel_hi:[0,1]
	v_lshlrev_b32_e32 v120, 16, v66
	v_and_b32_e32 v121, 0xffff0000, v66
	v_lshlrev_b32_e32 v66, 16, v67
	v_and_b32_e32 v67, 0xffff0000, v67
	v_pk_fma_f32 v[62:63], v[30:31], v[62:63], v[64:65]
	v_lshlrev_b32_e32 v64, 16, v110
	v_and_b32_e32 v65, 0xffff0000, v110
	v_pk_mul_f32 v[120:121], v[2:3], v[120:121] op_sel_hi:[0,1]
	v_lshlrev_b32_e32 v110, 16, v111
	v_and_b32_e32 v111, 0xffff0000, v111
	v_pk_mul_f32 v[66:67], v[2:3], v[66:67] op_sel_hi:[0,1]
	v_pk_fma_f32 v[64:65], v[32:33], v[120:121], v[64:65]
	v_pk_fma_f32 v[66:67], v[34:35], v[66:67], v[110:111]
	s_waitcnt vmcnt(0)
	s_andn2_b64 vcc, exec, s[44:45]
	s_cbranch_vccnz .LBB0_1370
	global_store_dwordx4 v[72:73], v[36:39], off offset:-4096
	global_store_dwordx4 v[72:73], v[40:43], off offset:-3072
	global_store_dwordx4 v[72:73], v[44:47], off offset:-2048
	global_store_dwordx4 v[72:73], v[48:51], off offset:-1024
	global_store_dwordx4 v[72:73], v[52:55], off
	global_store_dwordx4 v[72:73], v[56:59], off offset:1024
	global_store_dwordx4 v[72:73], v[60:63], off offset:2048
	global_store_dwordx4 v[72:73], v[64:67], off offset:3072
	s_cbranch_execnz .LBB0_1363
	s_branch .LBB0_1371
; #define GAS __attribute__((address_space(1)))
; __device__ __forceinline__ unsigned pk2(float lo, float hi) { f32x2_t_ v = {lo, hi}; bf16x2_t_ b = __builtin_convertvector(v, bf16x2_t_); return __builtin_bit_cast(unsigned, b); }
; __device__ __forceinline__ float quant_row(const f32x4 (&v)[8], unsigned char* xq, int lane) {
;     float mx = 0.f;
; #pragma unroll
;     for (int j = 0; j < 8; ++j) mx = __builtin_fmaxf(mx, __builtin_fmaxf(__builtin_fmaxf(__builtin_fabsf(v[j].x), __builtin_fabsf(v[j].y)), __builtin_fmaxf(__builtin_fabsf(v[j].z), __builtin_fabsf(v[j].w))));
;     mx = __builtin_fmaxf(wave_max(mx), 1e-20f);
; __device__ __forceinline__ void resid_rows(bf16* X, const bf16* Y, const float* PART, const float* gpost, float* RSv, float* RQv, float* fout, unsigned char* XQv, int m0, int mstep, int lane, int M_end = M) {
;     ...
;             s += (v[j].x * v[j].x + v[j].y * v[j].y) + (v[j].z * v[j].z + v[j].w * v[j].w); }
;         if (fout) { GAS f32x4* xo = (GAS f32x4*)(fout + (size_t)m * DM) + lane;
; #pragma unroll
;             for (int j = 0; j < 8; ++j) xo[64 * j] = v[j]; }
;         else { s = wave_sum(s); GAS v2u* xw = (GAS v2u*)(X + (size_t)m * DM) + lane;
; #pragma unroll
;             for (int j = 0; j < 8; ++j) { v2u w; w.x = pk2(v[j].x, v[j].y); w.y = pk2(v[j].z, v[j].w); xw[64 * j] = w; }
;             const float dq = quant_row(v, XQv + (size_t)m * DM, lane);
.LBB0_1370:
.LBB0_1371:
	v_pk_mul_f32 v[122:123], v[40:41], v[40:41]
	v_pk_mul_f32 v[124:125], v[42:43], v[42:43]
	v_pk_mul_f32 v[110:111], v[36:37], v[36:37]
	v_pk_mul_f32 v[120:121], v[38:39], v[38:39]
	v_add_f32_e32 v1, v125, v124
	v_add_f32_e32 v2, v122, v123
	v_add_f32_e32 v1, v2, v1
	v_add_f32_e32 v2, v121, v120
	v_add_f32_e32 v110, v110, v111
	v_pk_mul_f32 v[126:127], v[44:45], v[44:45]
	v_pk_mul_f32 v[128:129], v[46:47], v[46:47]
	v_add_f32_e32 v2, v110, v2
	v_add_f32_e32 v1, v2, v1
	v_add_f32_e32 v2, v129, v128
	v_add_f32_e32 v110, v126, v127
	v_pk_mul_f32 v[130:131], v[48:49], v[48:49]
	v_pk_mul_f32 v[132:133], v[50:51], v[50:51]
	v_add_f32_e32 v2, v110, v2
	v_add_f32_e32 v1, v2, v1
	v_add_f32_e32 v2, v133, v132
	v_add_f32_e32 v110, v130, v131
	v_pk_mul_f32 v[134:135], v[52:53], v[52:53]
	v_pk_mul_f32 v[136:137], v[54:55], v[54:55]
	v_add_f32_e32 v2, v110, v2
	v_add_f32_e32 v1, v2, v1
	v_add_f32_e32 v2, v137, v136
	v_add_f32_e32 v110, v134, v135
	v_pk_mul_f32 v[138:139], v[56:57], v[56:57]
	v_pk_mul_f32 v[140:141], v[58:59], v[58:59]
	v_add_f32_e32 v2, v110, v2
	v_add_f32_e32 v1, v2, v1
	v_add_f32_e32 v2, v141, v140
	v_add_f32_e32 v110, v138, v139
	v_pk_mul_f32 v[142:143], v[60:61], v[60:61]
	v_pk_mul_f32 v[144:145], v[62:63], v[62:63]
	v_add_f32_e32 v2, v110, v2
	v_add_f32_e32 v1, v2, v1
	v_add_f32_e32 v2, v145, v144
	v_add_f32_e32 v110, v142, v143
	v_pk_mul_f32 v[146:147], v[64:65], v[64:65]
	v_pk_mul_f32 v[148:149], v[66:67], v[66:67]
	v_add_f32_e32 v2, v110, v2
	v_add_f32_e32 v1, v2, v1
	v_add_f32_e32 v2, v149, v148
	v_add_f32_e32 v110, v146, v147
	v_add_f32_e32 v2, v110, v2
	v_add_f32_e32 v1, v2, v1
	s_nop 1
	v_add_f32_dpp v1, v1, v1 quad_perm:[1,0,3,2] row_mask:0xf bank_mask:0xf
	s_nop 1
	v_add_f32_dpp v1, v1, v1 quad_perm:[2,3,0,1] row_mask:0xf bank_mask:0xf
	s_nop 1
	v_add_f32_dpp v1, v1, v1 row_half_mirror row_mask:0xf bank_mask:0xf
	s_nop 1
	v_add_f32_dpp v1, v1, v1 row_mirror row_mask:0xf bank_mask:0xf
	s_nop 1
	v_readlane_b32 s100, v1, 0
	v_readlane_b32 s101, v1, 16
	s_nop 1
	v_mov_b32_e32 v210, s100
	v_add_f32_e32 v210, s101, v210
	v_readlane_b32 s100, v1, 32
	v_readlane_b32 s101, v1, 48
	s_nop 1
	v_add_f32_e32 v210, s100, v210
	v_add_f32_e32 v1, s101, v210
	v_max_f32_e64 v110, |v38|, |v38|
	v_max_f32_e64 v111, |v42|, |v42|
	v_max_f32_e64 v119, |v50|, |v50|
	s_mov_b32 s0, 0x23800000
	v_cvt_pk_bf16_f32 v120, v36, v37
	v_cvt_pk_bf16_f32 v121, v38, v39
	v_max_f32_e64 v2, |v39|, |v39|
	v_max_f32_e32 v2, v110, v2
	v_max_f32_e64 v110, |v43|, |v43|
	v_max_f32_e32 v110, v111, v110
	v_max3_f32 v2, |v36|, |v37|, v2
	v_max3_f32 v110, |v40|, |v41|, v110
	v_max3_f32 v2, v2, 0, v110
	v_max_f32_e64 v110, |v47|, |v47|
	v_max_f32_e64 v111, |v46|, |v46|
	v_max_f32_e32 v110, v111, v110
	v_max_f32_e64 v111, |v51|, |v51|
	v_max_f32_e32 v111, v119, v111
	v_max3_f32 v110, |v44|, |v45|, v110
	v_max3_f32 v111, |v48|, |v49|, v111
	v_max3_f32 v2, v2, v110, v111
	v_max_f32_e64 v110, |v55|, |v55|
	v_max_f32_e64 v111, |v54|, |v54|
	v_max_f32_e32 v110, v111, v110
	v_max_f32_e64 v111, |v59|, |v59|
	v_max_f32_e64 v119, |v58|, |v58|
	v_max_f32_e32 v111, v119, v111
	v_max3_f32 v110, |v52|, |v53|, v110
	v_max3_f32 v111, |v56|, |v57|, v111
	v_max3_f32 v2, v2, v110, v111
	v_max_f32_e64 v110, |v63|, |v63|
	v_max_f32_e64 v111, |v62|, |v62|
	v_max_f32_e32 v110, v111, v110
	v_max_f32_e64 v111, |v67|, |v67|
	v_max_f32_e64 v119, |v66|, |v66|
	v_max_f32_e32 v111, v119, v111
	v_max3_f32 v110, |v60|, |v61|, v110
	v_max3_f32 v111, |v64|, |v65|, v111
	v_max3_f32 v119, v2, v110, v111
	ds_bpermute_b32 v122, v113, v119
	v_lshl_add_u64 v[110:111], s[84:85], 0, v[70:71]
	s_waitcnt lgkmcnt(0)
	v_max_f32_e32 v122, v122, v122
	v_max_f32_e32 v119, v119, v122
	ds_bpermute_b32 v124, v114, v119
	v_add_co_u32_e32 v122, vcc, s0, v110
	v_cvt_pk_bf16_f32 v110, v40, v41
	s_nop 0
	v_addc_co_u32_e32 v123, vcc, 0, v111, vcc
	global_store_dwordx2 v[122:123], v[120:121], off
	s_waitcnt lgkmcnt(0)
	v_max_f32_e32 v120, v124, v124
	v_max_f32_e32 v119, v119, v120
	ds_bpermute_b32 v120, v115, v119
	v_cvt_pk_bf16_f32 v111, v42, v43
	global_store_dwordx2 v[122:123], v[110:111], off offset:512
	v_cvt_pk_bf16_f32 v110, v44, v45
	v_cvt_pk_bf16_f32 v111, v46, v47
	global_store_dwordx2 v[122:123], v[110:111], off offset:1024
	s_waitcnt lgkmcnt(0)
	v_max_f32_e32 v110, v120, v120
	v_max_f32_e32 v119, v119, v110
	ds_bpermute_b32 v120, v116, v119
	v_cvt_pk_bf16_f32 v110, v48, v49
	v_cvt_pk_bf16_f32 v111, v50, v51
	global_store_dwordx2 v[122:123], v[110:111], off offset:1536
	v_cvt_pk_bf16_f32 v110, v52, v53
	s_waitcnt lgkmcnt(0)
	v_max_f32_e32 v111, v120, v120
	v_max_f32_e32 v119, v119, v111
	ds_bpermute_b32 v120, v117, v119
	v_cvt_pk_bf16_f32 v111, v54, v55
	global_store_dwordx2 v[122:123], v[110:111], off offset:2048
	v_cvt_pk_bf16_f32 v110, v56, v57
	v_cvt_pk_bf16_f32 v111, v58, v59
	s_waitcnt lgkmcnt(0)
	v_max_f32_e32 v120, v120, v120
	v_max_f32_e32 v119, v119, v120
	ds_bpermute_b32 v120, v118, v119
	global_store_dwordx2 v[122:123], v[110:111], off offset:2560
	v_cvt_pk_bf16_f32 v110, v60, v61
	v_cvt_pk_bf16_f32 v111, v62, v63
	s_mov_b32 s0, 0x1e3ce508
	global_store_dwordx2 v[122:123], v[110:111], off offset:3072
	s_waitcnt lgkmcnt(0)
; #define GAS __attribute__((address_space(1)))
; __device__ __forceinline__ float quant_row(const f32x4 (&v)[8], unsigned char* xq, int lane) {
;     ...
;     mx = __builtin_fmaxf(wave_max(mx), 1e-20f);
;     const float q = 127.0f / mx;
;     GAS unsigned* o4 = (GAS unsigned*)xq + lane;
; #pragma unroll
;     for (int j = 0; j < 8; ++j) o4[64 * j] = q4(v[j], q);
;     return mx * (1.0f / 127.0f);
; __device__ __forceinline__ void resid_rows(bf16* X, const bf16* Y, const float* PART, const float* gpost, float* RSv, float* RQv, float* fout, unsigned char* XQv, int m0, int mstep, int lane, int M_end = M) {
;     ...
;             const float dq = quant_row(v, XQv + (size_t)m * DM, lane);
;             if (lane == 0) { const float r = 1.f / sqrtf(s * (1.f / DM) + NORM_EPS); RSv[m] = r; RQv[m] = r * dq; } }
	v_max3_f32 v110, v119, v120, s0
	s_mov_b32 s0, 0x42fe0000
	v_div_scale_f32 v111, s[18:19], v110, v110, s0
	v_rcp_f32_e32 v119, v111
	v_cvt_pk_bf16_f32 v120, v64, v65
	v_cvt_pk_bf16_f32 v121, v66, v67
	global_store_dwordx2 v[122:123], v[120:121], off offset:3584
	v_fma_f32 v120, -v111, v119, 1.0
	v_fmac_f32_e32 v119, v120, v119
	v_div_scale_f32 v120, vcc, s0, v110, s0
	v_mul_f32_e32 v121, v120, v119
	v_fma_f32 v122, -v111, v121, v120
	v_fmac_f32_e32 v121, v122, v119
	v_fma_f32 v111, -v111, v121, v120
	v_div_fmas_f32 v111, v111, v119, v121
	v_div_fixup_f32 v111, v111, v110, s0
	v_mul_f32_e32 v37, v37, v111
	v_mul_f32_e32 v36, v36, v111
	v_rndne_f32_e32 v37, v37
	v_mul_f32_e32 v38, v38, v111
	v_mul_f32_e32 v39, v39, v111
	v_rndne_f32_e32 v36, v36
	v_cvt_i32_f32_e32 v37, v37
	v_rndne_f32_e32 v38, v38
	v_rndne_f32_e32 v39, v39
	v_cvt_i32_f32_e32 v36, v36
	v_cvt_i32_f32_sdwa v38, v38 dst_sel:WORD_1 dst_unused:UNUSED_PAD src0_sel:DWORD
	v_cvt_i32_f32_e32 v39, v39
	v_lshlrev_b32_e32 v37, 8, v37
	v_lshl_add_u64 v[120:121], s[84:85], 0, v[68:69]
	v_and_b32_e32 v37, 0xff00, v37
	v_and_b32_e32 v38, 0xff0000, v38
	v_perm_b32 v36, v39, v36, s17
	s_mov_b32 s0, 0x8800000
	v_or3_b32 v38, v36, v37, v38
	v_add_co_u32_e32 v36, vcc, s0, v120
	v_mul_f32_e32 v39, v41, v111
	s_nop 0
	v_addc_co_u32_e32 v37, vcc, 0, v121, vcc
	global_store_dword v[36:37], v38, off
	v_mul_f32_e32 v38, v40, v111
	v_rndne_f32_e32 v39, v39
	v_mul_f32_e32 v40, v42, v111
	v_mul_f32_e32 v41, v43, v111
	v_rndne_f32_e32 v38, v38
	v_cvt_i32_f32_e32 v39, v39
	v_rndne_f32_e32 v40, v40
	v_rndne_f32_e32 v41, v41
	v_cvt_i32_f32_e32 v38, v38
	v_cvt_i32_f32_sdwa v40, v40 dst_sel:WORD_1 dst_unused:UNUSED_PAD src0_sel:DWORD
	v_cvt_i32_f32_e32 v41, v41
	v_lshlrev_b32_e32 v39, 8, v39
	v_and_b32_e32 v39, 0xff00, v39
	v_and_b32_e32 v40, 0xff0000, v40
	v_perm_b32 v38, v41, v38, s17
	v_or3_b32 v38, v38, v39, v40
	v_mul_f32_e32 v39, v45, v111
	global_store_dword v[36:37], v38, off offset:256
	v_mul_f32_e32 v38, v44, v111
	v_rndne_f32_e32 v39, v39
	v_mul_f32_e32 v40, v46, v111
	v_mul_f32_e32 v41, v47, v111
	v_rndne_f32_e32 v38, v38
	v_cvt_i32_f32_e32 v39, v39
	v_rndne_f32_e32 v40, v40
	v_rndne_f32_e32 v41, v41
	v_cvt_i32_f32_e32 v38, v38
	v_cvt_i32_f32_sdwa v40, v40 dst_sel:WORD_1 dst_unused:UNUSED_PAD src0_sel:DWORD
	v_cvt_i32_f32_e32 v41, v41
	v_lshlrev_b32_e32 v39, 8, v39
	v_and_b32_e32 v39, 0xff00, v39
	v_and_b32_e32 v40, 0xff0000, v40
	v_perm_b32 v38, v41, v38, s17
	v_or3_b32 v38, v38, v39, v40
	v_mul_f32_e32 v39, v49, v111
	global_store_dword v[36:37], v38, off offset:512
	v_mul_f32_e32 v38, v48, v111
	v_rndne_f32_e32 v39, v39
	v_mul_f32_e32 v40, v50, v111
	v_mul_f32_e32 v41, v51, v111
	v_rndne_f32_e32 v38, v38
	v_cvt_i32_f32_e32 v39, v39
	v_rndne_f32_e32 v40, v40
	v_rndne_f32_e32 v41, v41
	v_cvt_i32_f32_e32 v38, v38
	v_cvt_i32_f32_sdwa v40, v40 dst_sel:WORD_1 dst_unused:UNUSED_PAD src0_sel:DWORD
	v_cvt_i32_f32_e32 v41, v41
	v_lshlrev_b32_e32 v39, 8, v39
	v_and_b32_e32 v39, 0xff00, v39
	v_and_b32_e32 v40, 0xff0000, v40
	v_perm_b32 v38, v41, v38, s17
	v_or3_b32 v38, v38, v39, v40
	v_mul_f32_e32 v39, v53, v111
	global_store_dword v[36:37], v38, off offset:768
	v_mul_f32_e32 v38, v52, v111
	v_rndne_f32_e32 v39, v39
	v_mul_f32_e32 v40, v54, v111
	v_mul_f32_e32 v41, v55, v111
	v_rndne_f32_e32 v38, v38
	v_cvt_i32_f32_e32 v39, v39
	v_rndne_f32_e32 v40, v40
	v_rndne_f32_e32 v41, v41
	v_cvt_i32_f32_e32 v38, v38
	v_cvt_i32_f32_sdwa v40, v40 dst_sel:WORD_1 dst_unused:UNUSED_PAD src0_sel:DWORD
	v_cvt_i32_f32_e32 v41, v41
	v_lshlrev_b32_e32 v39, 8, v39
	v_and_b32_e32 v39, 0xff00, v39
	v_and_b32_e32 v40, 0xff0000, v40
	v_perm_b32 v38, v41, v38, s17
	v_or3_b32 v38, v38, v39, v40
	v_mul_f32_e32 v39, v57, v111
	global_store_dword v[36:37], v38, off offset:1024
	v_mul_f32_e32 v38, v56, v111
	v_rndne_f32_e32 v39, v39
	v_mul_f32_e32 v40, v58, v111
	v_mul_f32_e32 v41, v59, v111
	v_rndne_f32_e32 v38, v38
	v_cvt_i32_f32_e32 v39, v39
	v_rndne_f32_e32 v40, v40
	v_rndne_f32_e32 v41, v41
	v_cvt_i32_f32_e32 v38, v38
	v_cvt_i32_f32_sdwa v40, v40 dst_sel:WORD_1 dst_unused:UNUSED_PAD src0_sel:DWORD
	v_cvt_i32_f32_e32 v41, v41
	v_lshlrev_b32_e32 v39, 8, v39
	v_and_b32_e32 v39, 0xff00, v39
	v_and_b32_e32 v40, 0xff0000, v40
	v_perm_b32 v38, v41, v38, s17
	v_or3_b32 v38, v38, v39, v40
	v_mul_f32_e32 v39, v61, v111
	global_store_dword v[36:37], v38, off offset:1280
	v_mul_f32_e32 v38, v60, v111
	v_rndne_f32_e32 v39, v39
	v_mul_f32_e32 v40, v62, v111
	v_mul_f32_e32 v41, v63, v111
	v_rndne_f32_e32 v38, v38
	v_cvt_i32_f32_e32 v39, v39
	v_rndne_f32_e32 v40, v40
	v_rndne_f32_e32 v41, v41
	v_cvt_i32_f32_e32 v38, v38
	v_cvt_i32_f32_sdwa v40, v40 dst_sel:WORD_1 dst_unused:UNUSED_PAD src0_sel:DWORD
	v_cvt_i32_f32_e32 v41, v41
	v_lshlrev_b32_e32 v39, 8, v39
	v_and_b32_e32 v39, 0xff00, v39
	v_and_b32_e32 v40, 0xff0000, v40
	v_perm_b32 v38, v41, v38, s17
	v_or3_b32 v38, v38, v39, v40
	v_mul_f32_e32 v39, v65, v111
	global_store_dword v[36:37], v38, off offset:1536
	v_mul_f32_e32 v38, v64, v111
	v_rndne_f32_e32 v39, v39
	v_mul_f32_e32 v40, v66, v111
	v_mul_f32_e32 v41, v67, v111
	v_rndne_f32_e32 v38, v38
	v_cvt_i32_f32_e32 v39, v39
	v_rndne_f32_e32 v40, v40
	v_rndne_f32_e32 v41, v41
	v_cvt_i32_f32_e32 v38, v38
	v_cvt_i32_f32_sdwa v40, v40 dst_sel:WORD_1 dst_unused:UNUSED_PAD src0_sel:DWORD
	v_cvt_i32_f32_e32 v41, v41
	v_lshlrev_b32_e32 v39, 8, v39
	v_and_b32_e32 v39, 0xff00, v39
	v_and_b32_e32 v40, 0xff0000, v40
	v_perm_b32 v38, v41, v38, s17
	v_or3_b32 v38, v38, v39, v40
	global_store_dword v[36:37], v38, off offset:1792
	s_and_saveexec_b64 s[48:49], s[38:39]
	s_cbranch_execz .LBB0_1362
	v_fmamk_f32 v1, v1, 0x3a000000, v240
	v_mul_f32_e32 v2, 0x4f800000, v1
	v_cmp_gt_f32_e32 vcc, s82, v1
	s_nop 1
	v_cndmask_b32_e32 v1, v1, v2, vcc
	v_sqrt_f32_e32 v2, v1
	s_nop 0
	v_add_u32_e32 v36, -1, v2
	v_fma_f32 v38, -v36, v2, v1
	v_add_u32_e32 v37, 1, v2
	v_cmp_ge_f32_e64 s[40:41], 0, v38
	s_nop 1
	v_cndmask_b32_e64 v36, v2, v36, s[40:41]
	v_fma_f32 v2, -v37, v2, v1
	v_cmp_lt_f32_e64 s[40:41], 0, v2
	s_nop 1
	v_cndmask_b32_e64 v2, v36, v37, s[40:41]
	v_mul_f32_e32 v36, 0x37800000, v2
	v_cndmask_b32_e32 v2, v2, v36, vcc
	v_cmp_class_f32_e32 vcc, v1, v241
	v_mul_f32_e32 v37, 0x3c010204, v110
	s_nop 0
	v_cndmask_b32_e32 v1, v2, v1, vcc
	v_div_scale_f32 v2, s[18:19], v1, v1, 1.0
	v_rcp_f32_e32 v36, v2
	s_add_u32 s18, s84, s42
	s_addc_u32 s19, s85, s43
	v_fma_f32 v38, -v2, v36, 1.0
	v_fmac_f32_e32 v36, v38, v36
	v_div_scale_f32 v38, vcc, 1.0, v1, 1.0
	v_mul_f32_e32 v39, v38, v36
	v_fma_f32 v40, -v2, v39, v38
	v_fmac_f32_e32 v39, v40, v36
	v_fma_f32 v2, -v2, v39, v38
	v_div_fmas_f32 v2, v2, v36, v39
	v_div_fixup_f32 v1, v2, v1, 1.0
	global_store_dword v236, v1, s[18:19]
	v_mul_f32_e32 v1, v1, v37
	global_store_dword v237, v1, s[18:19]
	s_branch .LBB0_1362
